# attention loop: one bias MFMA per sub-tile + VALU fma(|b|,sgn,qk) instead of two MFMAs + med3 (20 vs 24 MFMAs per tile)
# speedup vs baseline: 1.0165x; 1.0098x over previous
.LBB2_18:
	s_or_b64 exec, exec, s[4:5]
	s_add_i32 s4, s52, 2
	s_lshr_b32 s49, s4, 1
	v_or_b32_e32 v99, 4, v89
	s_mov_b32 s48, 1
	s_cmp_eq_u32 s49, 1
	s_cbranch_scc1 .LBB2_32
	v_or_b32_e32 v1, s33, v37
	v_cmp_gt_u32_e64 s[36:37], v37, v31
	v_cmp_lt_u32_e64 s[4:5], v37, v31
	v_or_b32_e32 v31, 2, v1
	v_cmp_gt_u32_e64 s[6:7], v31, v35
	v_or_b32_e32 v31, 3, v1
	v_cmp_gt_u32_e64 s[8:9], v31, v35
	v_or_b32_e32 v31, 16, v1
	v_cmp_gt_u32_e64 s[10:11], v31, v35
	v_or_b32_e32 v31, 17, v1
	v_cmp_gt_u32_e64 s[12:13], v31, v35
	v_or_b32_e32 v31, 18, v1
	v_cmp_gt_u32_e64 s[14:15], v31, v35
	v_or_b32_e32 v31, 19, v1
	v_cmp_gt_u32_e64 s[16:17], v31, v35
	v_or_b32_e32 v31, 32, v1
	v_cmp_gt_u32_e64 s[18:19], v31, v35
	v_or_b32_e32 v31, 33, v1
	v_cmp_gt_u32_e64 s[20:21], v31, v35
	v_or_b32_e32 v31, 34, v1
	v_cmp_gt_u32_e64 s[22:23], v31, v35
	v_or_b32_e32 v31, 35, v1
	v_cmp_gt_u32_e64 s[24:25], v31, v35
	v_or_b32_e32 v31, 48, v1
	v_cmp_gt_u32_e64 s[26:27], v31, v35
	v_or_b32_e32 v31, 49, v1
	v_cmp_gt_u32_e64 s[28:29], v31, v35
	v_or_b32_e32 v31, 50, v1
	v_or_b32_e32 v1, 51, v1
	v_cmp_gt_u32_e64 s[34:35], v1, v35
	v_mov_b32_e32 v1, 0x100
	v_lshl_or_b32 v72, v88, 6, v1
	v_mov_b32_e32 v1, 0x4000
	v_lshl_or_b32 v70, v88, 12, v1
	v_mov_b32_e32 v1, 0x2000
	s_mov_b32 s44, 0x8000
	v_lshl_or_b32 v74, v88, 11, v1
	v_lshlrev_b32_e32 v78, 1, v30
	s_mov_b32 s45, 0x5040100
	v_xor_b32_e32 v1, 0x8000, v5
	v_xor_b32_sdwa v30, s44, v5 dst_sel:DWORD dst_unused:UNUSED_PAD src0_sel:DWORD src1_sel:WORD_1
	v_lshlrev_b32_e32 v101, 6, v33
	v_perm_b32 v33, v30, v1, s45
	v_xor_b32_e32 v1, 0x8000, v4
	v_xor_b32_sdwa v30, s44, v4 dst_sel:DWORD dst_unused:UNUSED_PAD src0_sel:DWORD src1_sel:WORD_1
	v_lshlrev_b32_e32 v76, 1, v32
	v_perm_b32 v32, v30, v1, s45
	v_xor_b32_e32 v1, 0x8000, v3
	v_xor_b32_sdwa v30, s44, v3 dst_sel:DWORD dst_unused:UNUSED_PAD src0_sel:DWORD src1_sel:WORD_1
	v_cmp_gt_u32_e64 s[30:31], v31, v35
	v_perm_b32 v31, v30, v1, s45
	v_xor_b32_e32 v1, 0x8000, v2
	v_xor_b32_sdwa v30, s44, v2 dst_sel:DWORD dst_unused:UNUSED_PAD src0_sel:DWORD src1_sel:WORD_1
	v_lshlrev_b32_e32 v100, 1, v88
	v_mov_b32_e32 v71, 0
	v_lshlrev_b32_e32 v102, 7, v40
	v_lshlrev_b32_e32 v103, 6, v40
	v_lshlrev_b32_e32 v104, 7, v39
	v_lshlrev_b32_e32 v105, 6, v39
	v_lshlrev_b32_e32 v106, 7, v38
	v_lshlrev_b32_e32 v107, 6, v38
	s_movk_i32 s50, 0x5000
	v_lshlrev_b32_e32 v80, 1, v36
	v_lshlrev_b32_e32 v82, 1, v34
	s_mov_b32 s51, 0xff800000
	s_mov_b32 s53, 0x41700000
	v_perm_b32 v30, v30, v1, s45
	v_mov_b32_e32 v108, 0xff800000
	v_readfirstlane_b32 s64, v98
	s_nop 0
	s_and_b32 s64, s64, 0x80000000
	s_or_b32 s64, s64, 0x3f800000

.LBB2_22:
	s_or_b64 exec, exec, s[44:45]
	v_cmp_ge_u32_e32 vcc, s52, v50
	s_and_saveexec_b64 s[44:45], vcc
	s_cbranch_execz .LBB2_29
	v_and_or_b32 v1, s48, 1, v100
	v_mul_u32_u24_e32 v46, 0x5000, v1
	v_or_b32_e32 v42, v46, v97
	v_add_u32_e32 v75, v42, v94
	ds_read_b128 v[34:37], v75
	v_add_u32_e32 v73, v42, v95
	ds_read_b128 v[42:45], v73
	v_sub_f32_e32 v38, 0x41000000, v69
	v_or_b32_e32 v47, v46, v96
	v_mov_b32_e32 v39, v38
	v_mov_b32_e32 v40, v38
	v_mov_b32_e32 v41, v38
	v_add_u32_e32 v48, v47, v101
	ds_read_b128 v[52:55], v48 offset:16384
	s_waitcnt lgkmcnt(0)
	v_mfma_f32_16x16x32_f16 v[34:37], v[34:37], v[6:9], v[38:41]
	v_or_b32_e32 v46, v46, v102
	v_cmp_eq_u32_e32 vcc, s52, v50
	v_mfma_f32_16x16x32_f16 v[34:37], v[42:45], v[10:13], v[34:37]
	v_add_u32_e32 v42, v46, v94
	ds_read_b128 v[42:45], v42
	v_add_u32_e32 v46, v46, v95
	v_mfma_f32_16x16x32_f16 v[56:59], v[52:55], v[2:5], 0
	ds_read_b128 v[52:55], v46
	v_add_u32_e32 v46, v47, v103
	ds_read_b128 v[60:63], v46 offset:16384
	s_waitcnt lgkmcnt(0)
	v_mfma_f32_16x16x32_f16 v[42:45], v[42:45], v[6:9], v[38:41]
	v_mad_u32_u24 v46, v1, s50, v104
	v_add_u32_e32 v48, v46, v94
	ds_read_b128 v[110:113], v48
	v_mfma_f32_16x16x32_f16 v[42:45], v[52:55], v[10:13], v[42:45]
	v_add_u32_e32 v46, v46, v95
	v_fma_f32 v34, |v56|, s64, v34
	v_fma_f32 v36, |v58|, s64, v36
	v_mfma_f32_16x16x32_f16 v[52:55], v[60:63], v[2:5], 0
	ds_read_b128 v[60:63], v46
	v_add_u32_e32 v46, v47, v105
	ds_read_b128 v[114:117], v46 offset:16384
	s_waitcnt lgkmcnt(0)
	v_mfma_f32_16x16x32_f16 v[110:113], v[110:113], v[6:9], v[38:41]
	v_mad_u32_u24 v46, v1, s50, v106
	v_add_u32_e32 v1, v46, v94
	v_mfma_f32_16x16x32_f16 v[60:63], v[60:63], v[10:13], v[110:113]
	s_nop 4
	ds_read_b128 v[110:113], v1
	v_fma_f32 v1, |v57|, s64, v35
	v_add_u32_e32 v35, v46, v95
	ds_read_b128 v[122:125], v35
	v_add_u32_e32 v35, v47, v107
	v_mfma_f32_16x16x32_f16 v[118:121], v[114:117], v[2:5], 0
	ds_read_b128 v[114:117], v35 offset:16384
	v_fma_f32 v35, |v59|, s64, v37
	v_fma_f32 v37, |v53|, s64, v43
	s_waitcnt lgkmcnt(0)
	v_mfma_f32_16x16x32_f16 v[110:113], v[110:113], v[6:9], v[38:41]
	v_mfma_f32_16x16x32_f16 v[56:59], v[122:125], v[10:13], v[110:113]
	s_nop 1
	v_fma_f32 v38, |v52|, s64, v42
	v_fma_f32 v40, |v54|, s64, v44
	v_fma_f32 v39, |v55|, s64, v45
	v_mfma_f32_16x16x32_f16 v[52:55], v[114:117], v[2:5], 0
	v_fma_f32 v42, |v118|, s64, v60
	v_fma_f32 v41, |v119|, s64, v61
	v_fma_f32 v44, |v120|, s64, v62
	v_fma_f32 v43, |v121|, s64, v63
	s_nop 6
	v_fma_f32 v46, |v52|, s64, v56
	v_fma_f32 v45, |v53|, s64, v57
	v_fma_f32 v48, |v54|, s64, v58
	v_fma_f32 v47, |v55|, s64, v59
	s_and_saveexec_b64 s[46:47], vcc
	s_cbranch_execz .LBB2_25
	v_mov_b32_e32 v50, s51
	v_cndmask_b32_e64 v50, v34, v50, s[36:37]
	v_cndmask_b32_e64 v34, v50, v34, s[4:5]
	v_mov_b32_e32 v50, s51
	v_cndmask_b32_e64 v1, v108, v1, s[4:5]
	v_cndmask_b32_e64 v36, v36, v108, s[6:7]
	v_cndmask_b32_e64 v35, v35, v108, s[8:9]
	v_cndmask_b32_e64 v38, v38, v50, s[10:11]
	v_cndmask_b32_e64 v37, v37, v108, s[12:13]
	v_cndmask_b32_e64 v40, v40, v108, s[14:15]
	v_cndmask_b32_e64 v39, v39, v108, s[16:17]
	v_cndmask_b32_e64 v42, v42, v50, s[18:19]
	v_cndmask_b32_e64 v41, v41, v108, s[20:21]
	v_cndmask_b32_e64 v44, v44, v108, s[22:23]
	v_cndmask_b32_e64 v43, v43, v108, s[24:25]
	v_cndmask_b32_e64 v46, v46, v50, s[26:27]
	v_cndmask_b32_e64 v45, v45, v108, s[28:29]
	v_cndmask_b32_e64 v48, v48, v108, s[30:31]
	v_cndmask_b32_e64 v47, v47, v108, s[34:35]

amdhsa.kernels:
  - .agpr_count:     0
    .args:
      - .actual_access:  read_only
        .address_space:  global
        .offset:         0
        .size:           8
        .value_kind:     global_buffer
      - .actual_access:  read_only
        .address_space:  global
        .offset:         8
        .size:           8
        .value_kind:     global_buffer
      - .actual_access:  read_only
        .address_space:  global
        .offset:         16
        .size:           8
        .value_kind:     global_buffer
      - .actual_access:  read_only
        .address_space:  global
        .offset:         24
        .size:           8
        .value_kind:     global_buffer
      - .actual_access:  read_only
        .address_space:  global
        .offset:         32
        .size:           8
        .value_kind:     global_buffer
      - .actual_access:  read_only
        .address_space:  global
        .offset:         40
        .size:           8
        .value_kind:     global_buffer
      - .actual_access:  read_only
        .address_space:  global
        .offset:         48
        .size:           8
        .value_kind:     global_buffer
      - .address_space:  global
        .offset:         56
        .size:           8
        .value_kind:     global_buffer
      - .address_space:  global
        .offset:         64
        .size:           8
        .value_kind:     global_buffer
      - .actual_access:  read_only
        .address_space:  global
        .offset:         72
        .size:           8
        .value_kind:     global_buffer
      - .address_space:  global
        .offset:         80
        .size:           8
        .value_kind:     global_buffer
    .group_segment_fixed_size: 0
    .kernarg_segment_align: 8
    .kernarg_segment_size: 88
    .language:       OpenCL C
    .language_version:
      - 2
      - 0
    .max_flat_workgroup_size: 256
    .name:           _Z11prep_kernelPKfS0_S0_S0_S0_S0_S0_PDF16_S1_S1_S1_
    .private_segment_fixed_size: 0
    .sgpr_count:     23
    .sgpr_spill_count: 0
    .symbol:         _Z11prep_kernelPKfS0_S0_S0_S0_S0_S0_PDF16_S1_S1_S1_.kd
    .uniform_work_group_size: 1
    .uses_dynamic_stack: false
    .vgpr_count:     28
    .vgpr_spill_count: 0
    .wavefront_size: 64
  - .agpr_count:     0
    .args:
      - .offset:         0
        .size:           88
        .value_kind:     by_value
    .group_segment_fixed_size: 163840
    .kernarg_segment_align: 8
    .kernarg_segment_size: 88
    .language:       OpenCL C
    .language_version:
      - 2
      - 0
    .max_flat_workgroup_size: 512
    .name:           _Z12gemm1_kernel6G1Args
    .private_segment_fixed_size: 0
    .sgpr_count:     58
    .sgpr_spill_count: 0
    .symbol:         _Z12gemm1_kernel6G1Args.kd
    .uniform_work_group_size: 1
    .uses_dynamic_stack: false
    .vgpr_count:     240
    .vgpr_spill_count: 0
    .wavefront_size: 64
  - .agpr_count:     0
    .args:
      - .address_space:  global
        .offset:         0
        .size:           8
        .value_kind:     global_buffer
      - .address_space:  global
        .offset:         8
        .size:           8
        .value_kind:     global_buffer
      - .address_space:  global
        .offset:         16
        .size:           8
        .value_kind:     global_buffer
      - .actual_access:  read_only
        .address_space:  global
        .offset:         24
        .size:           8
        .value_kind:     global_buffer
      - .actual_access:  read_only
        .address_space:  global
        .offset:         32
        .size:           8
        .value_kind:     global_buffer
      - .actual_access:  read_only
        .address_space:  global
        .offset:         40
        .size:           8
        .value_kind:     global_buffer
      - .address_space:  global
        .offset:         48
        .size:           8
        .value_kind:     global_buffer
      - .actual_access:  read_only
        .address_space:  global
        .offset:         56
        .size:           8
        .value_kind:     global_buffer
      - .address_space:  global
        .offset:         64
        .size:           8
        .value_kind:     global_buffer
      - .actual_access:  read_only
        .address_space:  global
        .offset:         72
        .size:           8
        .value_kind:     global_buffer
      - .address_space:  global
        .offset:         80
        .size:           8
        .value_kind:     global_buffer
    .group_segment_fixed_size: 81920
    .kernarg_segment_align: 8
    .kernarg_segment_size: 88
    .language:       OpenCL C
    .language_version:
      - 2
      - 0
    .max_flat_workgroup_size: 512
    .name:           _Z11attn_kernelPKDF16_S0_S0_PKfS2_S2_S0_S2_PDF16_S2_S3_
    .private_segment_fixed_size: 0
    .sgpr_count:     71
    .sgpr_spill_count: 0
    .symbol:         _Z11attn_kernelPKDF16_S0_S0_PKfS2_S2_S0_S2_PDF16_S2_S3_.kd
    .uniform_work_group_size: 1
    .uses_dynamic_stack: false
    .vgpr_count:     126
    .vgpr_spill_count: 0
    .wavefront_size: 64
  - .agpr_count:     0
    .args:
      - .address_space:  global
        .offset:         0
        .size:           8
        .value_kind:     global_buffer
      - .address_space:  global
        .offset:         8
        .size:           8
        .value_kind:     global_buffer
      - .actual_access:  read_only
        .address_space:  global
        .offset:         16
        .size:           8
        .value_kind:     global_buffer
      - .actual_access:  write_only
        .address_space:  global
        .offset:         24
        .size:           8
        .value_kind:     global_buffer
    .group_segment_fixed_size: 122880
    .kernarg_segment_align: 8
    .kernarg_segment_size: 32
    .language:       OpenCL C
    .language_version:
      - 2
      - 0
    .max_flat_workgroup_size: 512
    .name:           _Z14outproj_kernelPKDF16_S0_PKfPf
    .private_segment_fixed_size: 0
    .sgpr_count:     31
    .sgpr_spill_count: 0
    .symbol:         _Z14outproj_kernelPKDF16_S0_PKfPf.kd
    .uniform_work_group_size: 1
    .uses_dynamic_stack: false
    .vgpr_count:     132
    .vgpr_spill_count: 0
    .wavefront_size: 64
